# grid barrier: this CU's L1 invalidate issued before the spin/after the arrive atomic instead of after the release (on top of v2)
# baseline (speedup 1.0000x reference)
.LBB0_58:
	s_or_b64 exec, exec, s[12:13]
	v_cvt_f32_u32_e32 v5, v3
	s_waitcnt vmcnt(0)
	v_readfirstlane_b32 s3, v4
	v_sub_u32_e32 v4, 0, v3
	v_rcp_iflag_f32_e32 v5, v5
	v_add_u32_e32 v6, s3, v2
	v_mul_f32_e32 v5, 0x4f7ffffe, v5
	v_cvt_u32_f32_e32 v5, v5
	v_mul_lo_u32 v2, v4, v5
	v_mul_hi_u32 v2, v5, v2
	v_add_u32_e32 v2, v5, v2
	v_mul_hi_u32 v2, v6, v2
	v_mul_lo_u32 v4, v2, v3
	v_sub_u32_e32 v4, v6, v4
	v_add_u32_e32 v5, 1, v2
	v_cmp_ge_u32_e32 vcc, v4, v3
	s_nop 1
	v_cndmask_b32_e32 v2, v2, v5, vcc
	v_sub_u32_e32 v5, v4, v3
	v_cndmask_b32_e32 v4, v4, v5, vcc
	v_add_u32_e32 v5, 1, v2
	v_cmp_ge_u32_e32 vcc, v4, v3
	v_add_u32_e32 v4, 1, v6
	s_nop 0
	v_cndmask_b32_e32 v2, v2, v5, vcc
	v_mul_lo_u32 v5, v3, v2
	v_add_u32_e32 v3, v5, v3
	v_cmp_ne_u32_e32 vcc, v4, v3
	s_and_saveexec_b64 s[10:11], vcc
	s_xor_b64 s[10:11], exec, s[10:11]
	s_cbranch_execz .LBB0_72
	s_waitcnt lgkmcnt(0)
	v_mov_b32_e32 v1, 0x2000
	global_load_dword v1, v1, s[8:9] offset:1024 sc1
	buffer_inv sc1
	s_add_u32 s14, s8, 0x2400
	s_addc_u32 s15, s9, 0
	s_waitcnt vmcnt(0)
	v_cmp_eq_u32_e32 vcc, v1, v2
	s_and_saveexec_b64 s[12:13], vcc
	s_cbranch_execz .LBB0_71
	s_mov_b32 s3, 1
	s_mov_b64 s[16:17], 0
	v_mov_b32_e32 v1, 0
	s_branch .LBB0_62

.LBB0_71:
	s_or_b64 exec, exec, s[12:13]
	s_waitcnt vmcnt(0)
	s_waitcnt vmcnt(0)
.LBB0_72:
	s_andn2_saveexec_b64 s[10:11], s[10:11]
	s_cbranch_execz .LBB0_92
	s_mov_b64 s[10:11], exec
	buffer_wbl2 sc1
	s_waitcnt lgkmcnt(0)
	s_waitcnt vmcnt(0)
	v_mbcnt_lo_u32_b32 v2, s10, 0
	v_mbcnt_hi_u32_b32 v2, s11, v2
	v_cmp_eq_u32_e32 vcc, 0, v2
	s_and_saveexec_b64 s[12:13], vcc
	s_cbranch_execz .LBB0_75
	s_bcnt1_i32_b64 s3, s[10:11]
	v_mov_b32_e32 v3, 0x3000
	v_mov_b32_e32 v4, s3
	global_atomic_add v3, v3, v4, s[44:45] offset:1024 sc0
	buffer_inv sc1

.LBB0_89:
	s_or_b64 exec, exec, s[10:11]
	s_mov_b64 s[10:11], exec
	v_mbcnt_lo_u32_b32 v1, s10, 0
	v_mbcnt_hi_u32_b32 v1, s11, v1
	v_cmp_eq_u32_e32 vcc, 0, v1
	s_waitcnt vmcnt(0)
	s_and_saveexec_b64 s[12:13], vcc
	s_cbranch_execz .LBB0_91
	s_bcnt1_i32_b64 s3, s[10:11]
	v_mov_b32_e32 v1, 0x2000
	v_mov_b32_e32 v2, s3
	global_atomic_add v1, v2, s[8:9] offset:1024

.LBB0_256:
	s_or_b64 exec, exec, s[12:13]
	v_cvt_f32_u32_e32 v6, v4
	s_waitcnt vmcnt(0)
	v_readfirstlane_b32 s3, v5
	v_sub_u32_e32 v5, 0, v4
	v_rcp_iflag_f32_e32 v6, v6
	v_add_u32_e32 v7, s3, v3
	v_mul_f32_e32 v6, 0x4f7ffffe, v6
	v_cvt_u32_f32_e32 v6, v6
	v_mul_lo_u32 v3, v5, v6
	v_mul_hi_u32 v3, v6, v3
	v_add_u32_e32 v3, v6, v3
	v_mul_hi_u32 v3, v7, v3
	v_mul_lo_u32 v5, v3, v4
	v_sub_u32_e32 v5, v7, v5
	v_add_u32_e32 v6, 1, v3
	v_cmp_ge_u32_e32 vcc, v5, v4
	s_nop 1
	v_cndmask_b32_e32 v3, v3, v6, vcc
	v_sub_u32_e32 v6, v5, v4
	v_cndmask_b32_e32 v5, v5, v6, vcc
	v_add_u32_e32 v6, 1, v3
	v_cmp_ge_u32_e32 vcc, v5, v4
	v_add_u32_e32 v5, 1, v7
	s_nop 0
	v_cndmask_b32_e32 v3, v3, v6, vcc
	v_mul_lo_u32 v6, v4, v3
	v_add_u32_e32 v4, v6, v4
	v_cmp_ne_u32_e32 vcc, v5, v4
	s_and_saveexec_b64 s[10:11], vcc
	s_xor_b64 s[10:11], exec, s[10:11]
	s_cbranch_execz .LBB0_270
	s_waitcnt lgkmcnt(0)
	v_mov_b32_e32 v2, 0x2000
	global_load_dword v2, v2, s[8:9] offset:1024 sc1
	buffer_inv sc1
	s_add_u32 s14, s8, 0x2400
	s_addc_u32 s15, s9, 0
	s_waitcnt vmcnt(0)
	v_cmp_eq_u32_e32 vcc, v2, v3
	s_and_saveexec_b64 s[12:13], vcc
	s_cbranch_execz .LBB0_269
	s_mov_b32 s3, 1
	s_mov_b64 s[16:17], 0
	v_mov_b32_e32 v2, 0
	s_branch .LBB0_260

.LBB0_270:
	s_andn2_saveexec_b64 s[10:11], s[10:11]
	s_cbranch_execz .LBB0_290
	s_mov_b64 s[10:11], exec
	buffer_wbl2 sc1
	s_waitcnt lgkmcnt(0)
	s_waitcnt vmcnt(0)
	v_mbcnt_lo_u32_b32 v3, s10, 0
	v_mbcnt_hi_u32_b32 v3, s11, v3
	v_cmp_eq_u32_e32 vcc, 0, v3
	s_and_saveexec_b64 s[12:13], vcc
	s_cbranch_execz .LBB0_273
	s_bcnt1_i32_b64 s3, s[10:11]
	v_mov_b32_e32 v4, 0x3000
	v_mov_b32_e32 v5, s3
	global_atomic_add v4, v4, v5, s[44:45] offset:1024 sc0
	buffer_inv sc1

.LBB0_287:
	s_or_b64 exec, exec, s[10:11]
	s_mov_b64 s[10:11], exec
	v_mbcnt_lo_u32_b32 v2, s10, 0
	v_mbcnt_hi_u32_b32 v2, s11, v2
	v_cmp_eq_u32_e32 vcc, 0, v2
	s_waitcnt vmcnt(0)
	s_and_saveexec_b64 s[12:13], vcc
	s_cbranch_execz .LBB0_289
	s_bcnt1_i32_b64 s3, s[10:11]
	v_mov_b32_e32 v2, 0x2000
	v_mov_b32_e32 v3, s3
	global_atomic_add v2, v3, s[8:9] offset:1024

.LBB0_1490:
	s_or_b64 exec, exec, s[14:15]
	v_cvt_f32_u32_e32 v6, v4
	s_waitcnt vmcnt(0)
	v_readfirstlane_b32 s3, v5
	v_sub_u32_e32 v5, 0, v4
	v_rcp_iflag_f32_e32 v6, v6
	v_add_u32_e32 v7, s3, v3
	v_mul_f32_e32 v6, 0x4f7ffffe, v6
	v_cvt_u32_f32_e32 v6, v6
	v_mul_lo_u32 v3, v5, v6
	v_mul_hi_u32 v3, v6, v3
	v_add_u32_e32 v3, v6, v3
	v_mul_hi_u32 v3, v7, v3
	v_mul_lo_u32 v5, v3, v4
	v_sub_u32_e32 v5, v7, v5
	v_add_u32_e32 v6, 1, v3
	v_cmp_ge_u32_e32 vcc, v5, v4
	s_nop 1
	v_cndmask_b32_e32 v3, v3, v6, vcc
	v_sub_u32_e32 v6, v5, v4
	v_cndmask_b32_e32 v5, v5, v6, vcc
	v_add_u32_e32 v6, 1, v3
	v_cmp_ge_u32_e32 vcc, v5, v4
	v_add_u32_e32 v5, 1, v7
	s_nop 0
	v_cndmask_b32_e32 v3, v3, v6, vcc
	v_mul_lo_u32 v6, v4, v3
	v_add_u32_e32 v4, v6, v4
	v_cmp_ne_u32_e32 vcc, v5, v4
	s_and_saveexec_b64 s[12:13], vcc
	s_xor_b64 s[12:13], exec, s[12:13]
	s_cbranch_execz .LBB0_1504
	s_waitcnt lgkmcnt(0)
	v_mov_b32_e32 v2, 0x2000
	global_load_dword v2, v2, s[10:11] offset:1024 sc1
	buffer_inv sc1
	s_add_u32 s16, s10, 0x2400
	s_addc_u32 s17, s11, 0
	s_waitcnt vmcnt(0)
	v_cmp_eq_u32_e32 vcc, v2, v3
	s_and_saveexec_b64 s[14:15], vcc
	s_cbranch_execz .LBB0_1503
	s_mov_b32 s3, 1
	s_mov_b64 s[18:19], 0
	v_mov_b32_e32 v2, 0
	s_branch .LBB0_1494

.LBB0_1503:
	s_or_b64 exec, exec, s[14:15]
	s_waitcnt vmcnt(0)
	s_waitcnt vmcnt(0)
.LBB0_1504:
	s_andn2_saveexec_b64 s[12:13], s[12:13]
	s_cbranch_execz .LBB0_1524
	s_mov_b64 s[12:13], exec
	buffer_wbl2 sc1
	s_waitcnt lgkmcnt(0)
	s_waitcnt vmcnt(0)
	v_mbcnt_lo_u32_b32 v3, s12, 0
	v_mbcnt_hi_u32_b32 v3, s13, v3
	v_cmp_eq_u32_e32 vcc, 0, v3
	s_and_saveexec_b64 s[14:15], vcc
	s_cbranch_execz .LBB0_1507
	s_bcnt1_i32_b64 s3, s[12:13]
	v_mov_b32_e32 v4, 0x3000
	v_mov_b32_e32 v5, s3
	global_atomic_add v4, v4, v5, s[44:45] offset:1024 sc0
	buffer_inv sc1

.LBB0_1521:
	s_or_b64 exec, exec, s[12:13]
	s_mov_b64 s[12:13], exec
	v_mbcnt_lo_u32_b32 v2, s12, 0
	v_mbcnt_hi_u32_b32 v2, s13, v2
	v_cmp_eq_u32_e32 vcc, 0, v2
	s_waitcnt vmcnt(0)
	s_and_saveexec_b64 s[14:15], vcc
	s_cbranch_execz .LBB0_1523
	s_bcnt1_i32_b64 s3, s[12:13]
	v_mov_b32_e32 v2, 0x2000
	v_mov_b32_e32 v3, s3
	global_atomic_add v2, v3, s[10:11] offset:1024

.LBB0_1954:
	s_or_b64 exec, exec, s[12:13]
	v_cvt_f32_u32_e32 v6, v4
	s_waitcnt vmcnt(0)
	v_readfirstlane_b32 s10, v5
	v_sub_u32_e32 v5, 0, v4
	v_rcp_iflag_f32_e32 v6, v6
	v_add_u32_e32 v7, s10, v3
	v_mul_f32_e32 v6, 0x4f7ffffe, v6
	v_cvt_u32_f32_e32 v6, v6
	v_mul_lo_u32 v3, v5, v6
	v_mul_hi_u32 v3, v6, v3
	v_add_u32_e32 v3, v6, v3
	v_mul_hi_u32 v3, v7, v3
	v_mul_lo_u32 v5, v3, v4
	v_sub_u32_e32 v5, v7, v5
	v_add_u32_e32 v6, 1, v3
	v_cmp_ge_u32_e32 vcc, v5, v4
	s_nop 1
	v_cndmask_b32_e32 v3, v3, v6, vcc
	v_sub_u32_e32 v6, v5, v4
	v_cndmask_b32_e32 v5, v5, v6, vcc
	v_add_u32_e32 v6, 1, v3
	v_cmp_ge_u32_e32 vcc, v5, v4
	v_add_u32_e32 v5, 1, v7
	s_nop 0
	v_cndmask_b32_e32 v3, v3, v6, vcc
	v_mul_lo_u32 v6, v4, v3
	v_add_u32_e32 v4, v6, v4
	v_cmp_ne_u32_e32 vcc, v5, v4
	s_and_saveexec_b64 s[10:11], vcc
	s_xor_b64 s[10:11], exec, s[10:11]
	s_cbranch_execz .LBB0_1968
	s_waitcnt lgkmcnt(0)
	v_mov_b32_e32 v2, 0x2000
	global_load_dword v2, v2, s[8:9] offset:1024 sc1
	buffer_inv sc1
	s_add_u32 s14, s8, 0x2400
	s_addc_u32 s15, s9, 0
	s_waitcnt vmcnt(0)
	v_cmp_eq_u32_e32 vcc, v2, v3
	s_and_saveexec_b64 s[12:13], vcc
	s_cbranch_execz .LBB0_1967
	s_mov_b32 s26, 1
	s_mov_b64 s[16:17], 0
	v_mov_b32_e32 v2, 0
	s_branch .LBB0_1958

.LBB0_1968:
	s_andn2_saveexec_b64 s[10:11], s[10:11]
	s_cbranch_execz .LBB0_1988
	s_mov_b64 s[10:11], exec
	buffer_wbl2 sc1
	s_waitcnt lgkmcnt(0)
	s_waitcnt vmcnt(0)
	v_mbcnt_lo_u32_b32 v3, s10, 0
	v_mbcnt_hi_u32_b32 v3, s11, v3
	v_cmp_eq_u32_e32 vcc, 0, v3
	s_and_saveexec_b64 s[12:13], vcc
	s_cbranch_execz .LBB0_1971
	s_bcnt1_i32_b64 s10, s[10:11]
	v_mov_b32_e32 v4, 0x3000
	v_mov_b32_e32 v5, s10
	global_atomic_add v4, v4, v5, s[44:45] offset:1024 sc0
	buffer_inv sc1

.LBB0_1985:
	s_or_b64 exec, exec, s[10:11]
	s_mov_b64 s[10:11], exec
	v_mbcnt_lo_u32_b32 v2, s10, 0
	v_mbcnt_hi_u32_b32 v2, s11, v2
	v_cmp_eq_u32_e32 vcc, 0, v2
	s_waitcnt vmcnt(0)
	s_and_saveexec_b64 s[12:13], vcc
	s_cbranch_execz .LBB0_1987
	s_bcnt1_i32_b64 s10, s[10:11]
	v_mov_b32_e32 v2, 0x2000
	v_mov_b32_e32 v3, s10
	global_atomic_add v2, v3, s[8:9] offset:1024

.LBB0_2010:
	s_or_b64 exec, exec, s[10:11]
	v_cvt_f32_u32_e32 v6, v4
	s_waitcnt vmcnt(0)
	v_readfirstlane_b32 s8, v5
	v_sub_u32_e32 v5, 0, v4
	v_rcp_iflag_f32_e32 v6, v6
	v_add_u32_e32 v7, s8, v3
	v_mul_f32_e32 v6, 0x4f7ffffe, v6
	v_cvt_u32_f32_e32 v6, v6
	v_mul_lo_u32 v3, v5, v6
	v_mul_hi_u32 v3, v6, v3
	v_add_u32_e32 v3, v6, v3
	v_mul_hi_u32 v3, v7, v3
	v_mul_lo_u32 v5, v3, v4
	v_sub_u32_e32 v5, v7, v5
	v_add_u32_e32 v6, 1, v3
	v_cmp_ge_u32_e32 vcc, v5, v4
	s_nop 1
	v_cndmask_b32_e32 v3, v3, v6, vcc
	v_sub_u32_e32 v6, v5, v4
	v_cndmask_b32_e32 v5, v5, v6, vcc
	v_add_u32_e32 v6, 1, v3
	v_cmp_ge_u32_e32 vcc, v5, v4
	v_add_u32_e32 v5, 1, v7
	s_nop 0
	v_cndmask_b32_e32 v3, v3, v6, vcc
	v_mul_lo_u32 v6, v4, v3
	v_add_u32_e32 v4, v6, v4
	v_cmp_ne_u32_e32 vcc, v5, v4
	s_and_saveexec_b64 s[8:9], vcc
	s_xor_b64 s[8:9], exec, s[8:9]
	s_cbranch_execz .LBB0_2024
	s_waitcnt lgkmcnt(0)
	v_mov_b32_e32 v2, 0x2000
	global_load_dword v2, v2, s[6:7] offset:1024 sc1
	buffer_inv sc1
	s_add_u32 s12, s6, 0x2400
	s_addc_u32 s13, s7, 0
	s_waitcnt vmcnt(0)
	v_cmp_eq_u32_e32 vcc, v2, v3
	s_and_saveexec_b64 s[10:11], vcc
	s_cbranch_execz .LBB0_2023
	s_mov_b32 s24, 1
	s_mov_b64 s[14:15], 0
	v_mov_b32_e32 v2, 0
	s_branch .LBB0_2014

.LBB0_2023:
	s_or_b64 exec, exec, s[10:11]
	s_waitcnt vmcnt(0)
	s_waitcnt vmcnt(0)
.LBB0_2024:
	s_andn2_saveexec_b64 s[8:9], s[8:9]
	s_cbranch_execz .LBB0_2044
	s_mov_b64 s[8:9], exec
	buffer_wbl2 sc1
	s_waitcnt lgkmcnt(0)
	s_waitcnt vmcnt(0)
	v_mbcnt_lo_u32_b32 v3, s8, 0
	v_mbcnt_hi_u32_b32 v3, s9, v3
	v_cmp_eq_u32_e32 vcc, 0, v3
	s_and_saveexec_b64 s[10:11], vcc
	s_cbranch_execz .LBB0_2027
	s_bcnt1_i32_b64 s8, s[8:9]
	v_mov_b32_e32 v4, 0x3000
	v_mov_b32_e32 v5, s8
	global_atomic_add v4, v4, v5, s[44:45] offset:1024 sc0
	buffer_inv sc1

.LBB0_2041:
	s_or_b64 exec, exec, s[8:9]
	s_mov_b64 s[8:9], exec
	v_mbcnt_lo_u32_b32 v2, s8, 0
	v_mbcnt_hi_u32_b32 v2, s9, v2
	v_cmp_eq_u32_e32 vcc, 0, v2
	s_waitcnt vmcnt(0)
	s_and_saveexec_b64 s[10:11], vcc
	s_cbranch_execz .LBB0_2043
	s_bcnt1_i32_b64 s8, s[8:9]
	v_mov_b32_e32 v2, 0x2000
	v_mov_b32_e32 v3, s8
	global_atomic_add v2, v3, s[6:7] offset:1024

.LBB0_2102:
	s_or_b64 exec, exec, s[8:9]
	v_cvt_f32_u32_e32 v5, v3
	s_waitcnt vmcnt(0)
	v_readfirstlane_b32 s6, v4
	v_sub_u32_e32 v4, 0, v3
	v_rcp_iflag_f32_e32 v5, v5
	v_add_u32_e32 v6, s6, v2
	v_mul_f32_e32 v5, 0x4f7ffffe, v5
	v_cvt_u32_f32_e32 v5, v5
	v_mul_lo_u32 v2, v4, v5
	v_mul_hi_u32 v2, v5, v2
	v_add_u32_e32 v2, v5, v2
	v_mul_hi_u32 v2, v6, v2
	v_mul_lo_u32 v4, v2, v3
	v_sub_u32_e32 v4, v6, v4
	v_add_u32_e32 v5, 1, v2
	v_cmp_ge_u32_e32 vcc, v4, v3
	s_nop 1
	v_cndmask_b32_e32 v2, v2, v5, vcc
	v_sub_u32_e32 v5, v4, v3
	v_cndmask_b32_e32 v4, v4, v5, vcc
	v_add_u32_e32 v5, 1, v2
	v_cmp_ge_u32_e32 vcc, v4, v3
	v_add_u32_e32 v4, 1, v6
	s_nop 0
	v_cndmask_b32_e32 v2, v2, v5, vcc
	v_mul_lo_u32 v5, v3, v2
	v_add_u32_e32 v3, v5, v3
	v_cmp_ne_u32_e32 vcc, v4, v3
	s_and_saveexec_b64 s[6:7], vcc
	s_xor_b64 s[6:7], exec, s[6:7]
	s_cbranch_execz .LBB0_2116
	s_waitcnt lgkmcnt(0)
	v_mov_b32_e32 v1, 0x2000
	global_load_dword v1, v1, s[4:5] offset:1024 sc1
	buffer_inv sc1
	s_add_u32 s10, s4, 0x2400
	s_addc_u32 s11, s5, 0
	s_waitcnt vmcnt(0)
	v_cmp_eq_u32_e32 vcc, v1, v2
	s_and_saveexec_b64 s[8:9], vcc
	s_cbranch_execz .LBB0_2115
	s_mov_b32 s22, 1
	s_mov_b64 s[12:13], 0
	v_mov_b32_e32 v1, 0
	s_branch .LBB0_2106

.LBB0_2115:
	s_or_b64 exec, exec, s[8:9]
	s_waitcnt vmcnt(0)
	s_waitcnt vmcnt(0)
.LBB0_2116:
	s_andn2_saveexec_b64 s[6:7], s[6:7]
	s_cbranch_execz .LBB0_2136
	s_mov_b64 s[6:7], exec
	buffer_wbl2 sc1
	s_waitcnt lgkmcnt(0)
	s_waitcnt vmcnt(0)
	v_mbcnt_lo_u32_b32 v2, s6, 0
	v_mbcnt_hi_u32_b32 v2, s7, v2
	v_cmp_eq_u32_e32 vcc, 0, v2
	s_and_saveexec_b64 s[8:9], vcc
	s_cbranch_execz .LBB0_2119
	s_bcnt1_i32_b64 s6, s[6:7]
	v_mov_b32_e32 v3, 0x3000
	v_mov_b32_e32 v4, s6
	global_atomic_add v3, v3, v4, s[44:45] offset:1024 sc0
	buffer_inv sc1

.LBB0_2133:
	s_or_b64 exec, exec, s[6:7]
	s_mov_b64 s[6:7], exec
	v_mbcnt_lo_u32_b32 v1, s6, 0
	v_mbcnt_hi_u32_b32 v1, s7, v1
	v_cmp_eq_u32_e32 vcc, 0, v1
	s_waitcnt vmcnt(0)
	s_and_saveexec_b64 s[8:9], vcc
	s_cbranch_execz .LBB0_2135
	s_bcnt1_i32_b64 s6, s[6:7]
	v_mov_b32_e32 v1, 0x2000
	v_mov_b32_e32 v2, s6
	global_atomic_add v1, v2, s[4:5] offset:1024
